# MLA fast88 loop: second P.V MFMA of each tile deferred to the start of the next half-iteration (fills the barrier-to-first-QK gap); non-visible waves zero P; on top of the K-fragment read hoist
# speedup vs baseline: 1.0088x; 1.0088x over previous
; #define ALAS __attribute__((address_space(3)))
; #define ATT_WAIT_BAR() asm volatile("s_waitcnt vmcnt(0) lgkmcnt(0)\n\ts_barrier" ::: "memory")
; #define MF_ISSUE_K(t, s) do { glds16(ksrc + (long)(t) * 64 * 512, (unsigned)__builtin_amdgcn_readfirstlane(kdst + (s) * KSLOT)); \
;         if (wid < 4) glds16(krsrc + (long)(t) * 64 * 32, (unsigned)__builtin_amdgcn_readfirstlane(krdst + (s) * KSLOT)); } while (0)
; __device__ __forceinline__ bool mla_unit_fast88(const Args& A, int b, int h, int qb, ALAS char* shm, const int tidb) {
;     ...
;     const int t_end = 4 * qb + 4;
;     const int cw = 4 * qb + (wid >> 1);
;     if (tid == 0) bailw[0] = 0;
;     MF_ISSUE_K(0, 0); MF_ISSUE_V(0, 0); MF_ISSUE_K(1, 1);
;     const unsigned char* Q8w = A.Q8 + (rowbase + q0 + wid * 32 + r32) * 768 + h * 96;
;     const unsigned char* Q8r = hi == 0 ? Q8w + 64 : A.ZERO;
;     v8i qf0, qf1;
;     { const u32x4 a0 = *(const u32x4*)(Q8w + 32 * hi), a1 = *(const u32x4*)(Q8w + 32 * hi + 16), b0 = *(const u32x4*)(Q8r), b1 = *(const u32x4*)(Q8r + 16);
;       qf0 = (v8i){(int)a0.x, (int)a0.y, (int)a0.z, (int)a0.w, (int)a1.x, (int)a1.y, (int)a1.z, (int)a1.w}; qf1 = (v8i){(int)b0.x, (int)b0.y, (int)b0.z, (int)b0.w, (int)b1.x, (int)b1.y, (int)b1.z, (int)b1.w}; }
;     const int sa8 = 0x7c7c7c7c, sb8 = 0x7b7b7b7b;
;     f32x16 o0 = {}, o1 = {}, ls = {};
;     const v8i ones8 = {0x38383838, 0x38383838, 0x38383838, 0x38383838, 0x38383838, 0x38383838, 0x38383838, 0x38383838};
;     const int vbo = ((lane >> 4) & 1) * 32 + (lane & 3) * 8 + (4 * hi + ((lane & 15) >> 2)) * 64;
;     ALAS const char* Kfr = shm + L_K + lane * 16;
;     ...
;     ATT_WAIT_BAR();
;     f32x16 cs[2][2];
;     { f32x16 z0 = {}, z1 = {}; ALAS const char* Ks_ = Kfr;
;       v8i k00, k01, k10, k11; M8_KFRAG(k00, Ks_, 0, 0); M8_KFRAG(k01, Ks_, 0, 1); M8_KFRAG(k10, Ks_, 1, 0); M8_KFRAG(k11, Ks_, 1, 1);
;       mfma8_acc(z0, k00, qf0, sa8, sb8); mfma8_acc(z1, k01, qf0, sa8, sb8); mfma8_acc(z0, k10, qf1, sa8, sb8); mfma8_acc(z1, k11, qf1, sa8, sb8);
;       asm volatile("s_nop 15\n\ts_nop 7" : "+v"(z0), "+v"(z1));
;       cs[0][0] = z0; cs[0][1] = z1; }
;     const float mhat = MF_ROWMAX(cs[0][0], cs[0][1]);
; #pragma unroll
;     for (int r = 0; r < 16; ++r) { cs[0][0][r] -= mhat; cs[0][1][r] -= mhat; }
;     f32x16 negm;
; #pragma unroll
;     for (int r = 0; r < 16; ++r) negm[r] = -mhat;
;     bool bailed = false; int ks = 0, vs = 0;
.LBB0_648:
	v_cmp_gt_u32_e32 vcc, 32, v154
	v_mov_b32_e32 v2, 0x800
	v_mov_b32_e32 v3, 0x8000
	v_cndmask_b32_e32 v2, 0, v2, vcc
	v_cndmask_b32_e64 v100, v2, v3, s[2:3]
	s_lshl_b32 s2, s6, 8
	v_mov_b32_e32 v101, v1
	s_lshl_b32 s37, s6, 2
	s_add_i32 s3, s45, 0x2000
	s_or_b32 s36, s30, s2
	s_lshl_b32 s2, s1, 5
	s_add_i32 s0, s37, 4
	s_add_i32 s47, s47, s37
	v_lshl_add_u64 v[2:3], v[146:147], 0, v[100:101]
	s_mov_b32 s4, m0
	s_mov_b32 m0, s3
	s_nop 0
	global_load_lds_dwordx4 v[2:3], off
	s_mov_b32 m0, s4
	s_ashr_i32 s3, s2, 31
	s_add_u32 s24, s36, s2
	v_or_b32_e32 v4, s24, v156
	v_mov_b64_e32 v[2:3], s[74:75]
	s_addc_u32 s25, s31, s3
	v_mad_u64_u32 v[2:3], s[2:3], v4, s67, v[2:3]
	v_mov_b32_e32 v4, 0x300
	v_mad_i32_i24 v3, s25, v4, v3
	v_lshl_add_u64 v[4:5], v[2:3], 0, 64
	v_mov_b32_e32 v6, s27
	v_cndmask_b32_e32 v5, v6, v5, vcc
	v_mov_b32_e32 v6, s26
	v_lshl_add_u64 v[2:3], v[2:3], 0, v[0:1]
	v_cndmask_b32_e32 v4, v6, v4, vcc
	global_load_dwordx4 v[134:137], v[2:3], off offset:16
	global_load_dwordx4 v[130:133], v[2:3], off
	global_load_dwordx4 v[142:145], v[4:5], off offset:16
	global_load_dwordx4 v[138:141], v[4:5], off
	v_lshlrev_b32_e32 v155, 4, v154
	s_mov_b32 s4, 0
	v_add_u32_e32 v157, 0, v155
	s_waitcnt vmcnt(0) lgkmcnt(0)
	s_barrier
	s_mov_b32 s18, s4
	s_mov_b32 s19, s4
	ds_read_b128 v[50:53], v157
	ds_read_b128 v[54:57], v157 offset:1024
	ds_read_b128 v[58:61], v157 offset:2048
	ds_read_b128 v[62:65], v157 offset:3072
	ds_read_b128 v[66:69], v157 offset:4096
	ds_read_b128 v[70:73], v157 offset:5120
	ds_read_b128 v[74:77], v157 offset:6144
	ds_read_b128 v[78:81], v157 offset:7168
	s_mov_b32 s5, s4
	s_mov_b32 s6, s4
	s_mov_b32 s7, s4
	s_mov_b32 s8, s4
	s_mov_b32 s9, s4
	s_mov_b32 s10, s4
	s_mov_b32 s11, s4
	s_mov_b32 s12, s4
	s_mov_b32 s13, s4
	s_mov_b32 s14, s4
	s_mov_b32 s15, s4
	s_mov_b32 s16, s4
	s_mov_b32 s17, s4
	v_mov_b64_e32 v[32:33], s[18:19]
	v_mov_b64_e32 v[30:31], s[16:17]
	v_mov_b64_e32 v[28:29], s[14:15]
	v_mov_b64_e32 v[26:27], s[12:13]
	v_mov_b64_e32 v[24:25], s[10:11]
	v_mov_b64_e32 v[22:23], s[8:9]
	v_mov_b64_e32 v[20:21], s[6:7]
	v_mov_b64_e32 v[18:19], s[4:5]
	v_mov_b64_e32 v[48:49], v[32:33]
	v_mov_b64_e32 v[46:47], v[30:31]
	v_mov_b64_e32 v[44:45], v[28:29]
	v_mov_b64_e32 v[42:43], v[26:27]
	v_mov_b64_e32 v[40:41], v[24:25]
	v_mov_b64_e32 v[38:39], v[22:23]
	v_mov_b64_e32 v[36:37], v[20:21]
	v_mov_b64_e32 v[34:35], v[18:19]
	v_mov_b32_e32 v16, v1
	v_mov_b32_e32 v17, v1
	v_mov_b32_e32 v2, v1
	v_mov_b32_e32 v3, v1
	v_mov_b32_e32 v4, v1
	v_mov_b32_e32 v5, v1
	v_mov_b32_e32 v6, v1
	v_mov_b32_e32 v7, v1
	v_mov_b32_e32 v8, v1
	v_mov_b32_e32 v9, v1
	v_mov_b32_e32 v10, v1
	v_mov_b32_e32 v11, v1
	v_mov_b32_e32 v12, v1
	v_mov_b32_e32 v13, v1
	v_mov_b32_e32 v14, v1
	v_mov_b32_e32 v15, v1
	s_mov_b32 s41, s31
	s_mov_b32 s5, 3
	v_mul_hi_u32_u24_e32 v149, 3, v100
	v_mul_u32_u24_e32 v148, 3, v100
	v_lshl_add_u64 v[150:151], v[98:99], 0, s[78:79]
	s_waitcnt vmcnt(0) lgkmcnt(0)
	v_mfma_scale_f32_32x32x64_f8f6f4 v[34:49], v[50:57], v[130:137], v[34:49], v247, v253 op_sel_hi:[0,0,0]
	s_waitcnt lgkmcnt(4)
	v_mfma_scale_f32_32x32x64_f8f6f4 v[18:33], v[58:65], v[130:137], v[18:33], v247, v253 op_sel_hi:[0,0,0]
	s_waitcnt vmcnt(0) lgkmcnt(2)
	v_mfma_scale_f32_32x32x64_f8f6f4 v[34:49], v[66:73], v[138:145], v[34:49], v247, v253 op_sel_hi:[0,0,0]
	s_waitcnt lgkmcnt(0)
	v_mfma_scale_f32_32x32x64_f8f6f4 v[18:33], v[74:81], v[138:145], v[18:33], v247, v253 op_sel_hi:[0,0,0]
	s_nop 0
	s_nop 15
	s_nop 7
	s_nop 0
	v_max3_f32 v0, v34, v18, v38
	s_nop 0
	v_max3_f32 v0, v0, v22, v42
	s_nop 0
	v_max3_f32 v0, v0, v26, v46
	s_nop 0
	v_max_f32_e32 v0, v0, v30
	v_max3_f32 v50, v35, v19, v39
	s_nop 0
	v_max3_f32 v50, v50, v23, v43
	s_nop 0
	v_max3_f32 v50, v50, v27, v47
	s_nop 0
	v_max_f32_e32 v50, v50, v31
	v_max3_f32 v51, v36, v20, v40
	s_nop 0
	v_max3_f32 v51, v51, v24, v44
	s_nop 0
	v_max3_f32 v51, v51, v28, v48
	s_nop 0
	v_max_f32_e32 v51, v51, v32
	v_max3_f32 v52, v37, v21, v41
	s_nop 0
	v_max3_f32 v52, v52, v25, v45
	s_nop 0
	v_max3_f32 v52, v52, v29, v49
	s_nop 0
	v_max_f32_e32 v52, v52, v33
	v_max3_f32 v0, v0, v50, v51
	s_nop 0
	v_max_f32_e32 v0, v0, v52
	s_nop 0
	v_mov_b32_e32 v50, v0
	s_nop 1
	v_permlane32_swap_b32_e32 v0, v50
	v_max_f32_e32 v50, v50, v50
	v_max_f32_e32 v0, v0, v0
	v_max_f32_e32 v0, v0, v50
	v_sub_f32_e32 v65, v49, v0
	v_sub_f32_e32 v64, v48, v0
	v_sub_f32_e32 v63, v47, v0
	v_sub_f32_e32 v62, v46, v0
	v_sub_f32_e32 v61, v45, v0
	v_sub_f32_e32 v60, v44, v0
	v_sub_f32_e32 v59, v43, v0
	v_sub_f32_e32 v58, v42, v0
	v_sub_f32_e32 v57, v41, v0
	v_sub_f32_e32 v56, v40, v0
	v_sub_f32_e32 v55, v39, v0
	v_sub_f32_e32 v54, v38, v0
	v_sub_f32_e32 v53, v37, v0
	v_sub_f32_e32 v52, v36, v0
	v_sub_f32_e32 v51, v35, v0
	v_sub_f32_e32 v50, v34, v0
	v_sub_f32_e32 v97, v33, v0
	v_sub_f32_e32 v96, v32, v0
	v_sub_f32_e32 v95, v31, v0
	v_sub_f32_e32 v94, v30, v0
	v_sub_f32_e32 v93, v29, v0
	v_sub_f32_e32 v92, v28, v0
	v_sub_f32_e32 v91, v27, v0
	v_sub_f32_e32 v90, v26, v0
	v_sub_f32_e32 v89, v25, v0
	v_sub_f32_e32 v88, v24, v0
	v_sub_f32_e32 v87, v23, v0
	v_sub_f32_e32 v86, v22, v0
	v_sub_f32_e32 v85, v21, v0
	v_sub_f32_e32 v84, v20, v0
	v_sub_f32_e32 v83, v19, v0
	v_sub_f32_e32 v82, v18, v0
	v_xor_b32_e32 v66, 0x80000000, v0
	v_mov_b64_e32 v[32:33], v[16:17]
	v_mov_b64_e32 v[48:49], v[16:17]
	v_mov_b32_e32 v67, v66
	v_mov_b32_e32 v68, v66
	v_mov_b32_e32 v69, v66
	v_mov_b32_e32 v70, v66
	v_mov_b32_e32 v71, v66
	v_mov_b32_e32 v72, v66
	v_mov_b32_e32 v73, v66
	v_mov_b32_e32 v74, v66
	v_mov_b32_e32 v75, v66
	v_mov_b32_e32 v76, v66
	v_mov_b32_e32 v77, v66
	v_mov_b32_e32 v78, v66
	v_mov_b32_e32 v79, v66
	v_mov_b32_e32 v80, v66
	v_mov_b32_e32 v81, v66
	v_lshlrev_b32_e32 v0, 1, v100
	v_mov_b64_e32 v[30:31], v[14:15]
	v_mov_b64_e32 v[28:29], v[12:13]
	v_mov_b64_e32 v[26:27], v[10:11]
	v_mov_b64_e32 v[24:25], v[8:9]
	v_mov_b64_e32 v[22:23], v[6:7]
	v_mov_b64_e32 v[20:21], v[4:5]
	v_mov_b64_e32 v[18:19], v[2:3]
	v_mov_b64_e32 v[46:47], v[14:15]
	v_mov_b64_e32 v[44:45], v[12:13]
	v_mov_b64_e32 v[42:43], v[10:11]
	v_mov_b64_e32 v[40:41], v[8:9]
	v_mov_b64_e32 v[38:39], v[6:7]
	v_mov_b64_e32 v[36:37], v[4:5]
	v_mov_b64_e32 v[34:35], v[2:3]
	v_mov_b32_e32 v172, 0
	v_mov_b32_e32 v173, 0
	v_mov_b32_e32 v174, 0
	v_mov_b32_e32 v175, 0
	v_mov_b32_e32 v176, 0
	v_mov_b32_e32 v177, 0
	v_mov_b32_e32 v178, 0
	v_mov_b32_e32 v179, 0
	v_mov_b32_e32 v180, 0
	v_mov_b32_e32 v181, 0
	v_mov_b32_e32 v182, 0
	v_mov_b32_e32 v183, 0
	v_mov_b32_e32 v184, 0
	v_mov_b32_e32 v185, 0
	v_mov_b32_e32 v186, 0
	v_mov_b32_e32 v187, 0
; #define ALAS __attribute__((address_space(3)))
; #define MF_ISSUE_K(t, s) do { glds16(ksrc + (long)(t) * 64 * 512, (unsigned)__builtin_amdgcn_readfirstlane(kdst + (s) * KSLOT)); \
;         if (wid < 4) glds16(krsrc + (long)(t) * 64 * 32, (unsigned)__builtin_amdgcn_readfirstlane(krdst + (s) * KSLOT)); } while (0)
; #define MF_ISSUE_V(t, s) glds16(vsrc + (long)(t) * 64 * 512, (unsigned)__builtin_amdgcn_readfirstlane(vdst + (s) * VSLOT))
; #define MF_ISSUE_K(t, s) glds16(ks8 + (long)(t) * kst8, (unsigned)__builtin_amdgcn_readfirstlane(kdst + (s) * KSLOT))
; #define MF_ISSUE_V(t, s) glds16(vsrc + (long)(t) * 64 * 512, (unsigned)__builtin_amdgcn_readfirstlane(vdst + (s) * VSLOT))
; #define M8_KFRAG(dst, base, m, kh) do { const u32x4 lo_ = *(ALAS const u32x4*)((base) + (((m) * 2 + (kh)) * 2) * 1024), hi_ = *(ALAS const u32x4*)((base) + (((m) * 2 + (kh)) * 2 + 1) * 1024); \
;         dst = (v8i){(int)lo_.x, (int)lo_.y, (int)lo_.z, (int)lo_.w, (int)hi_.x, (int)hi_.y, (int)hi_.z, (int)hi_.w}; } while (0)
; #define MF_ISSUE_K(t, s) glds16(ks8 + (long)(t) * kst8, (unsigned)__builtin_amdgcn_readfirstlane(kdst + (s) * KSLOT))
; #define MF_ISSUE_V(t, s) do { if (wid < 4) glds16(vs8 + (long)(t) * 4096, (unsigned)__builtin_amdgcn_readfirstlane(vdst + (s) * 4096)); } while (0)
; #define M8_KFRAG(dst, base, m, kh) do { const u32x4 lo_ = *(ALAS const u32x4*)((base) + (((m) * 2 + (kh)) * 2) * 1024), hi_ = *(ALAS const u32x4*)((base) + (((m) * 2 + (kh)) * 2 + 1) * 1024); \
;         dst = (v8i){(int)lo_.x, (int)lo_.y, (int)lo_.z, (int)lo_.w, (int)hi_.x, (int)hi_.y, (int)hi_.z, (int)hi_.w}; } while (0)
; __device__ __forceinline__ bool mla_unit_fast88(const Args& A, int b, int h, int qb, ALAS char* shm, const int tidb) {
;     ...
;             const int ks1 = ks == 2 ? 0 : ks + 1, ks2 = ks1 == 2 ? 0 : ks1 + 1;
;             if (t + 2 < t_end) MF_ISSUE_K(t + 2, ks2);
;             if (t + 1 < t_end) MF_ISSUE_V(t + 1, vs ^ 1);
;             if (vis) {
;                 {
;                     ALAS const char* Ks_ = Kfr + ks1 * KSLOT;
;                     v8i kfa, kfb; M8_KFRAG(kfa, Ks_, 0, 0);
;                     M8_KFRAG(kfb, Ks_, 0, 1);
;     ...
;                 mfma8p_acc(o1, pf, vf1, 0x7f7f7f7f, 0x7c7c7c7c);
.LBB0_649:
	s_add_i32 s2, s4, 1
	s_cmp_lg_u32 s4, 2
	s_cselect_b32 s4, s2, 0
	v_lshl_add_u32 v171, s4, 13, v157
	ds_read_b128 v[114:117], v171
	ds_read_b128 v[118:121], v171 offset:1024
	ds_read_b128 v[164:167], v171 offset:2048
	ds_read_b128 v[168:171], v171 offset:3072
	v_mfma_scale_f32_32x32x64_f8f6f4 v[18:33], v[180:187], v[172:179], v[18:33], v251, v247 op_sel_hi:[0,0,0] cbsz:1
	s_add_i32 s6, s5, -1
	s_cmp_lt_u32 s6, s0
	s_cselect_b64 s[2:3], -1, 0
	s_and_b64 vcc, exec, s[2:3]
	v_lshl_add_u64 v[152:153], v[146:147], 0, v[0:1]
	s_cbranch_vccz .LBB0_651
	s_lshl_b32 s7, s4, 13
	s_addk_i32 s7, 0x2000
	s_cmp_lg_u32 s4, 2
	s_cselect_b32 s7, s7, 0
	v_lshl_add_u64 v[158:159], v[146:147], 0, v[0:1]
	s_add_i32 s7, s7, s45
	s_mov_b32 s8, m0
	s_mov_b32 m0, s7
	s_nop 0
	global_load_lds_dwordx4 v[158:159], off
	s_mov_b32 m0, s8

; #define ALAS __attribute__((address_space(3)))
; __device__ __forceinline__ bool mla_unit_fast88(const Args& A, int b, int h, int qb, ALAS char* shm, const int tidb) {
;     ...
;             if (vis) {
;                 {
;                     ALAS const char* Ks_ = Kfr + ks1 * KSLOT;
;                     v8i kfa, kfb; M8_KFRAG(kfa, Ks_, 0, 0);
;                     M8_KFRAG(kfb, Ks_, 0, 1);
;                     mfma8_new(N0, kfa, qf0, negm, sa8, sb8);
; #pragma unroll
;                     for (int e = 0; e < 8; ++e) C0[e] = __builtin_amdgcn_exp2f(C0[e]);
;                     __builtin_amdgcn_sched_barrier(0);
;                     M8_KFRAG(kfa, Ks_, 1, 0);
;                     mfma8_new(N1, kfb, qf0, negm, sa8, sb8);
; #pragma unroll
;                     for (int e = 8; e < 16; ++e) C0[e] = __builtin_amdgcn_exp2f(C0[e]);
;                     __builtin_amdgcn_sched_barrier(0);
;                     M8_KFRAG(kfb, Ks_, 1, 1);
;                     mfma8_acc(N0, kfa, qf1, sa8, sb8);
; #pragma unroll
;                     for (int e = 0; e < 8; ++e) C1[e] = __builtin_amdgcn_exp2f(C1[e]);
;                     __builtin_amdgcn_sched_barrier(0);
;                     mfma8_acc(N1, kfb, qf1, sa8, sb8);
; #pragma unroll
;                     for (int e = 8; e < 16; ++e) C1[e] = __builtin_amdgcn_exp2f(C1[e]);
;                     __builtin_amdgcn_sched_barrier(0);
;                 }
;                 ALAS const char* vb_ = shm + L_V + vs * 4096 + lane * 16;
;                 v8i vf0, vf1;
;                 { const u32x4 a0 = *(ALAS const u32x4*)(vb_), a1 = *(ALAS const u32x4*)(vb_ + 1024), b0 = *(ALAS const u32x4*)(vb_ + 2048), b1 = *(ALAS const u32x4*)(vb_ + 3072);
;                   vf0 = (v8i){(int)a0.x, (int)a0.y, (int)a0.z, (int)a0.w, (int)a1.x, (int)a1.y, (int)a1.z, (int)a1.w}; vf1 = (v8i){(int)b0.x, (int)b0.y, (int)b0.z, (int)b0.w, (int)b1.x, (int)b1.y, (int)b1.z, (int)b1.w}; }
;                 v8i pf;
; #pragma unroll
;                 for (int kk = 0; kk < 4; ++kk) { const f32x16& cc_ = (kk < 2) ? C0 : C1; const int k8_ = 8 * (kk & 1);
;                     int w0_ = 0, w1_ = 0;
;                     w0_ = __builtin_amdgcn_cvt_pk_bf8_f32(cc_[k8_], cc_[k8_ + 1], w0_, false); w0_ = __builtin_amdgcn_cvt_pk_bf8_f32(cc_[k8_ + 2], cc_[k8_ + 3], w0_, true);
.LBB0_653:
	s_add_i32 s7, s5, -3
	s_cmp_gt_i32 s7, s47
	s_cbranch_scc1 .Lmla_nv0
	v_lshl_add_u32 v158, s4, 13, v157
	v_exp_f32_e32 v50, v50
	v_exp_f32_e32 v51, v51
	v_exp_f32_e32 v52, v52
	v_exp_f32_e32 v53, v53
	v_exp_f32_e32 v54, v54
	v_exp_f32_e32 v55, v55
	v_exp_f32_e32 v56, v56
	v_exp_f32_e32 v57, v57
	s_waitcnt lgkmcnt(2)
	v_mfma_scale_f32_32x32x64_f8f6f4 v[98:113], v[114:121], v[130:137], v[66:81], v247, v253 op_sel_hi:[0,0,0]
	ds_read_b128 v[172:175], v158 offset:4096
	ds_read_b128 v[176:179], v158 offset:5120
	v_exp_f32_e32 v58, v58
	v_exp_f32_e32 v59, v59
	v_exp_f32_e32 v60, v60
	v_exp_f32_e32 v61, v61
	v_exp_f32_e32 v62, v62
	v_exp_f32_e32 v63, v63
	v_exp_f32_e32 v64, v64
	v_exp_f32_e32 v65, v65
	s_waitcnt lgkmcnt(2)
	v_mfma_scale_f32_32x32x64_f8f6f4 v[114:129], v[164:171], v[130:137], v[66:81], v247, v253 op_sel_hi:[0,0,0]
	ds_read_b128 v[164:167], v158 offset:6144
	ds_read_b128 v[168:171], v158 offset:7168
	v_exp_f32_e32 v82, v82
	v_exp_f32_e32 v83, v83
	v_exp_f32_e32 v84, v84
	v_exp_f32_e32 v85, v85
	v_exp_f32_e32 v86, v86
	v_exp_f32_e32 v87, v87
	v_exp_f32_e32 v88, v88
	v_exp_f32_e32 v89, v89
	s_waitcnt lgkmcnt(2)
	v_mfma_scale_f32_32x32x64_f8f6f4 v[98:113], v[172:179], v[138:145], v[98:113], v247, v253 op_sel_hi:[0,0,0]
	v_exp_f32_e32 v90, v90
	v_exp_f32_e32 v91, v91
	v_exp_f32_e32 v92, v92
	v_exp_f32_e32 v93, v93
	v_exp_f32_e32 v94, v94
	v_exp_f32_e32 v95, v95
	v_exp_f32_e32 v96, v96
	v_exp_f32_e32 v97, v97
	s_waitcnt lgkmcnt(0)
	v_mfma_scale_f32_32x32x64_f8f6f4 v[114:129], v[164:171], v[138:145], v[114:129], v247, v253 op_sel_hi:[0,0,0]
	ds_read_b128 v[164:167], v157 offset:36864
	ds_read_b128 v[168:171], v157 offset:37888
	ds_read_b128 v[172:175], v157 offset:38912
	ds_read_b128 v[176:179], v157 offset:39936
	v_mov_b32_e32 v180, 0
	v_mov_b32_e32 v181, 0
	v_mov_b32_e32 v182, 0
	v_mov_b32_e32 v183, 0
	v_mov_b32_e32 v184, 0
	v_mov_b32_e32 v185, 0
	v_mov_b32_e32 v186, 0
	v_mov_b32_e32 v187, 0
	v_cvt_pk_bf8_f32 v180, v50, v51
	v_cvt_pk_bf8_f32 v181, v54, v55
	v_cvt_pk_bf8_f32 v182, v58, v59
	v_cvt_pk_bf8_f32 v183, v62, v63
	v_cvt_pk_bf8_f32 v184, v82, v83
	v_cvt_pk_bf8_f32 v185, v86, v87
	v_cvt_pk_bf8_f32 v186, v90, v91
	v_cvt_pk_bf8_f32 v187, v94, v95
	v_cvt_pk_bf8_f32 v180, v52, v53 op_sel:[0,0,1]
	v_cvt_pk_bf8_f32 v181, v56, v57 op_sel:[0,0,1]
	v_cvt_pk_bf8_f32 v182, v60, v61 op_sel:[0,0,1]
	v_cvt_pk_bf8_f32 v183, v64, v65 op_sel:[0,0,1]
	v_cvt_pk_bf8_f32 v184, v84, v85 op_sel:[0,0,1]
	v_cvt_pk_bf8_f32 v185, v88, v89 op_sel:[0,0,1]
	v_cvt_pk_bf8_f32 v186, v92, v93 op_sel:[0,0,1]
	v_cvt_pk_bf8_f32 v187, v96, v97 op_sel:[0,0,1]
	s_waitcnt lgkmcnt(2)
	v_mfma_scale_f32_32x32x64_f8f6f4 v[2:17], v[180:187], v[164:171], v[2:17], v251, v247 op_sel_hi:[0,0,0] cbsz:1
	s_waitcnt lgkmcnt(0)
	v_mov_b32_e32 v163, v162
	v_mov_b32_e32 v164, v162
	v_mov_b32_e32 v165, v162
	v_mov_b32_e32 v166, v162
	v_mov_b32_e32 v167, v162
	v_mov_b32_e32 v168, v162
	v_mov_b32_e32 v169, v162
	v_mfma_scale_f32_32x32x64_f8f6f4 v[34:49], v[180:187], v[162:169], v[34:49], v251, v251 op_sel_hi:[0,0,0] cbsz:1
.LBB0_655:
	s_add_i32 s8, s4, 1
	s_waitcnt vmcnt(0) lgkmcnt(0)
	s_barrier
	s_cmp_lg_u32 s4, 2
	s_cselect_b32 s4, s8, 0
	v_lshl_add_u32 v171, s4, 13, v157
	ds_read_b128 v[82:85], v171
	ds_read_b128 v[86:89], v171 offset:1024
	ds_read_b128 v[164:167], v171 offset:2048
	ds_read_b128 v[168:171], v171 offset:3072
	v_mfma_scale_f32_32x32x64_f8f6f4 v[18:33], v[180:187], v[172:179], v[18:33], v251, v247 op_sel_hi:[0,0,0] cbsz:1
	s_cmp_ge_u32 s5, s0
	s_cbranch_scc1 .LBB0_661
	s_lshl_b32 s8, s4, 13
	s_addk_i32 s8, 0x2000
	s_cmp_lg_u32 s4, 2
	s_cselect_b32 s8, s8, 0
	v_lshl_add_u64 v[146:147], v[146:147], 0, v[148:149]
	s_add_i32 s8, s8, s45
	s_mov_b32 s9, m0
	s_mov_b32 m0, s8
	s_nop 0
	global_load_lds_dwordx4 v[146:147], off
	s_mov_b32 m0, s9
	s_and_b64 s[2:3], s[34:35], s[2:3]
	s_andn2_b64 vcc, exec, s[2:3]
	s_cbranch_vccz .LBB0_662

; #define ALAS __attribute__((address_space(3)))
; __device__ __forceinline__ bool mla_unit_fast88(const Args& A, int b, int h, int qb, ALAS char* shm, const int tidb) {
;     ...
;             if (vis) {
;                 {
;                     ALAS const char* Ks_ = Kfr + ks1 * KSLOT;
;                     v8i kfa, kfb; M8_KFRAG(kfa, Ks_, 0, 0);
;                     M8_KFRAG(kfb, Ks_, 0, 1);
;                     mfma8_new(N0, kfa, qf0, negm, sa8, sb8);
; #pragma unroll
;                     for (int e = 0; e < 8; ++e) C0[e] = __builtin_amdgcn_exp2f(C0[e]);
;                     __builtin_amdgcn_sched_barrier(0);
;                     M8_KFRAG(kfa, Ks_, 1, 0);
;                     mfma8_new(N1, kfb, qf0, negm, sa8, sb8);
; #pragma unroll
;                     for (int e = 8; e < 16; ++e) C0[e] = __builtin_amdgcn_exp2f(C0[e]);
;                     __builtin_amdgcn_sched_barrier(0);
;                     M8_KFRAG(kfb, Ks_, 1, 1);
;                     mfma8_acc(N0, kfa, qf1, sa8, sb8);
; #pragma unroll
;                     for (int e = 0; e < 8; ++e) C1[e] = __builtin_amdgcn_exp2f(C1[e]);
;                     __builtin_amdgcn_sched_barrier(0);
;                     mfma8_acc(N1, kfb, qf1, sa8, sb8);
; #pragma unroll
;                     for (int e = 8; e < 16; ++e) C1[e] = __builtin_amdgcn_exp2f(C1[e]);
;                     __builtin_amdgcn_sched_barrier(0);
;                 }
;                 ALAS const char* vb_ = shm + L_V + vs * 4096 + lane * 16;
;                 v8i vf0, vf1;
;                 { const u32x4 a0 = *(ALAS const u32x4*)(vb_), a1 = *(ALAS const u32x4*)(vb_ + 1024), b0 = *(ALAS const u32x4*)(vb_ + 2048), b1 = *(ALAS const u32x4*)(vb_ + 3072);
;                   vf0 = (v8i){(int)a0.x, (int)a0.y, (int)a0.z, (int)a0.w, (int)a1.x, (int)a1.y, (int)a1.z, (int)a1.w}; vf1 = (v8i){(int)b0.x, (int)b0.y, (int)b0.z, (int)b0.w, (int)b1.x, (int)b1.y, (int)b1.z, (int)b1.w}; }
;                 v8i pf;
; #pragma unroll
;                 for (int kk = 0; kk < 4; ++kk) { const f32x16& cc_ = (kk < 2) ? C0 : C1; const int k8_ = 8 * (kk & 1);
;                     int w0_ = 0, w1_ = 0;
;                     w0_ = __builtin_amdgcn_cvt_pk_bf8_f32(cc_[k8_], cc_[k8_ + 1], w0_, false); w0_ = __builtin_amdgcn_cvt_pk_bf8_f32(cc_[k8_ + 2], cc_[k8_ + 3], w0_, true);
.LBB0_658:
	v_lshl_add_u32 v146, s4, 13, v157
	v_exp_f32_e32 v98, v98
	v_exp_f32_e32 v99, v99
	v_exp_f32_e32 v100, v100
	v_exp_f32_e32 v101, v101
	v_exp_f32_e32 v102, v102
	v_exp_f32_e32 v103, v103
	v_exp_f32_e32 v104, v104
	v_exp_f32_e32 v105, v105
	s_waitcnt lgkmcnt(2)
	v_mfma_scale_f32_32x32x64_f8f6f4 v[50:65], v[82:89], v[130:137], v[66:81], v247, v253 op_sel_hi:[0,0,0]
	ds_read_b128 v[172:175], v146 offset:4096
	ds_read_b128 v[176:179], v146 offset:5120
	v_exp_f32_e32 v106, v106
	v_exp_f32_e32 v107, v107
	v_exp_f32_e32 v108, v108
	v_exp_f32_e32 v109, v109
	v_exp_f32_e32 v110, v110
	v_exp_f32_e32 v111, v111
	v_exp_f32_e32 v112, v112
	v_exp_f32_e32 v113, v113
	s_waitcnt lgkmcnt(2)
	v_mfma_scale_f32_32x32x64_f8f6f4 v[82:97], v[164:171], v[130:137], v[66:81], v247, v253 op_sel_hi:[0,0,0]
	ds_read_b128 v[164:167], v146 offset:6144
	ds_read_b128 v[168:171], v146 offset:7168
	v_exp_f32_e32 v114, v114
	v_exp_f32_e32 v115, v115
	v_exp_f32_e32 v116, v116
	v_exp_f32_e32 v117, v117
	v_exp_f32_e32 v118, v118
	v_exp_f32_e32 v119, v119
	v_exp_f32_e32 v120, v120
	v_exp_f32_e32 v121, v121
	s_waitcnt lgkmcnt(2)
	v_mfma_scale_f32_32x32x64_f8f6f4 v[50:65], v[172:179], v[138:145], v[50:65], v247, v253 op_sel_hi:[0,0,0]
	v_exp_f32_e32 v122, v122
	v_exp_f32_e32 v123, v123
	v_exp_f32_e32 v124, v124
	v_exp_f32_e32 v125, v125
	v_exp_f32_e32 v126, v126
	v_exp_f32_e32 v127, v127
	v_exp_f32_e32 v128, v128
	v_exp_f32_e32 v129, v129
	s_waitcnt lgkmcnt(0)
	v_mfma_scale_f32_32x32x64_f8f6f4 v[82:97], v[164:171], v[138:145], v[82:97], v247, v253 op_sel_hi:[0,0,0]
	ds_read_b128 v[164:167], v157 offset:40960
	ds_read_b128 v[168:171], v157 offset:41984
	ds_read_b128 v[172:175], v157 offset:43008
	ds_read_b128 v[176:179], v157 offset:44032
	v_mov_b32_e32 v180, 0
	v_mov_b32_e32 v181, 0
	v_mov_b32_e32 v182, 0
	v_mov_b32_e32 v183, 0
	v_mov_b32_e32 v184, 0
	v_mov_b32_e32 v185, 0
	v_mov_b32_e32 v186, 0
	v_mov_b32_e32 v187, 0
	v_cvt_pk_bf8_f32 v180, v98, v99
	v_cvt_pk_bf8_f32 v181, v102, v103
	v_cvt_pk_bf8_f32 v182, v106, v107
	v_cvt_pk_bf8_f32 v183, v110, v111
	v_cvt_pk_bf8_f32 v184, v114, v115
	v_cvt_pk_bf8_f32 v185, v118, v119
	v_cvt_pk_bf8_f32 v186, v122, v123
	v_cvt_pk_bf8_f32 v187, v126, v127
	v_cvt_pk_bf8_f32 v180, v100, v101 op_sel:[0,0,1]
	v_cvt_pk_bf8_f32 v181, v104, v105 op_sel:[0,0,1]
	v_cvt_pk_bf8_f32 v182, v108, v109 op_sel:[0,0,1]
	v_cvt_pk_bf8_f32 v183, v112, v113 op_sel:[0,0,1]
	v_cvt_pk_bf8_f32 v184, v116, v117 op_sel:[0,0,1]
	v_cvt_pk_bf8_f32 v185, v120, v121 op_sel:[0,0,1]
	v_cvt_pk_bf8_f32 v186, v124, v125 op_sel:[0,0,1]
	v_cvt_pk_bf8_f32 v187, v128, v129 op_sel:[0,0,1]
	s_waitcnt lgkmcnt(2)
	v_mfma_scale_f32_32x32x64_f8f6f4 v[2:17], v[180:187], v[164:171], v[2:17], v251, v247 op_sel_hi:[0,0,0] cbsz:1
	s_waitcnt lgkmcnt(0)
	v_mov_b32_e32 v163, v162
	v_mov_b32_e32 v164, v162
	v_mov_b32_e32 v165, v162
	v_mov_b32_e32 v166, v162
	v_mov_b32_e32 v167, v162
	v_mov_b32_e32 v168, v162
	v_mov_b32_e32 v169, v162
	v_mfma_scale_f32_32x32x64_f8f6f4 v[34:49], v[180:187], v[162:169], v[34:49], v251, v251 op_sel_hi:[0,0,0] cbsz:1

; #define MF_ISSUE_K(t, s) do { glds16(ksrc + (long)(t) * 64 * 512, (unsigned)__builtin_amdgcn_readfirstlane(kdst + (s) * KSLOT)); \
;         if (wid < 4) glds16(krsrc + (long)(t) * 64 * 32, (unsigned)__builtin_amdgcn_readfirstlane(krdst + (s) * KSLOT)); } while (0)
; #define MF_ISSUE_V(t, s) glds16(vsrc + (long)(t) * 64 * 512, (unsigned)__builtin_amdgcn_readfirstlane(vdst + (s) * VSLOT))
; #define MF_ISSUE_K(t, s) glds16(ks8 + (long)(t) * kst8, (unsigned)__builtin_amdgcn_readfirstlane(kdst + (s) * KSLOT))
; #define MF_ISSUE_V(t, s) glds16(vsrc + (long)(t) * 64 * 512, (unsigned)__builtin_amdgcn_readfirstlane(vdst + (s) * VSLOT))
; #define MF_ISSUE_K(t, s) glds16(ks8 + (long)(t) * kst8, (unsigned)__builtin_amdgcn_readfirstlane(kdst + (s) * KSLOT))
; #define MF_ISSUE_V(t, s) do { if (wid < 4) glds16(vs8 + (long)(t) * 4096, (unsigned)__builtin_amdgcn_readfirstlane(vdst + (s) * 4096)); } while (0)
; __device__ __forceinline__ bool mla_unit_fast88(const Args& A, int b, int h, int qb, ALAS char* shm, const int tidb) {
;     ...
;             const int t = t2 + p; f32x16 &C0 = cs[p][0], &C1 = cs[p][1], &N0 = cs[p ^ 1][0], &N1 = cs[p ^ 1][1];
;             const bool vis = !bailed && t <= cw;
;             const int ks1 = ks == 2 ? 0 : ks + 1, ks2 = ks1 == 2 ? 0 : ks1 + 1;
;             if (t + 2 < t_end) MF_ISSUE_K(t + 2, ks2);
;             if (t + 1 < t_end) MF_ISSUE_V(t + 1, vs ^ 1);
;             if (vis) {
.Lmla_nv0:
	v_mov_b32_e32 v180, 0
	v_mov_b32_e32 v181, 0
	v_mov_b32_e32 v182, 0
	v_mov_b32_e32 v183, 0
	v_mov_b32_e32 v184, 0
	v_mov_b32_e32 v185, 0
	v_mov_b32_e32 v186, 0
	v_mov_b32_e32 v187, 0
	s_branch .LBB0_655

; __device__ __forceinline__ int crow(int r, int hi) { return (r & 3) + 8 * (r >> 2) + 4 * hi; }
; #define ATT_WAIT_BAR() asm volatile("s_waitcnt vmcnt(0) lgkmcnt(0)\n\ts_barrier" ::: "memory")
; __device__ __forceinline__ bool mla_unit_fast88(const Args& A, int b, int h, int qb, ALAS char* shm, const int tidb) {
;     ...
;                 mfma8p_acc(o1, pf, vf1, 0x7f7f7f7f, 0x7c7c7c7c);
;                 mfma8p_acc(ls, pf, ones8, 0x7f7f7f7f, 0x7f7f7f7f);
;                 __builtin_amdgcn_sched_barrier(0);
;             }
;             ks = ks1; vs ^= 1;
;             ATT_WAIT_BAR();
;         }
;     }
;     asm volatile("s_nop 15\n\ts_nop 15" : "+v"(o0), "+v"(o1), "+v"(ls));
;     { bool bad_ = false;
; #pragma unroll
;       for (int r = 0; r < 16; ++r) bad_ |= !(ls[r] > 1.0e-30f && ls[r] < 5.7e4f);
;       if (__any(bad_)) bailed = true; }
;     if (bailed && lane == 0) bailw[0] = 1;
;     if (r32 == 0) {
; #pragma unroll
;         for (int r = 0; r < 16; ++r) wsf[32 + crow(r, hi)] = ls[r]; }
.LBB0_665:
	v_mfma_scale_f32_32x32x64_f8f6f4 v[18:33], v[180:187], v[172:179], v[18:33], v251, v247 op_sel_hi:[0,0,0] cbsz:1
	s_mov_b32 s6, 0x475ea800
	s_nop 15
	s_nop 15
	s_nop 0
	v_cmp_nlt_f32_e32 vcc, s39, v34
	v_cmp_ngt_f32_e64 s[2:3], s6, v34
	s_or_b64 s[4:5], vcc, s[2:3]
	v_cmp_nlt_f32_e32 vcc, s39, v35
	v_cmp_ngt_f32_e64 s[2:3], s6, v35
	s_or_b64 s[2:3], vcc, s[2:3]
	s_or_b64 s[4:5], s[4:5], s[2:3]
	v_cmp_nlt_f32_e32 vcc, s39, v36
	v_cmp_ngt_f32_e64 s[2:3], s6, v36
	s_or_b64 s[2:3], vcc, s[2:3]
	s_or_b64 s[4:5], s[2:3], s[4:5]
	v_cmp_nlt_f32_e32 vcc, s39, v37
	v_cmp_ngt_f32_e64 s[2:3], s6, v37
	s_or_b64 s[2:3], vcc, s[2:3]
	s_or_b64 s[4:5], s[2:3], s[4:5]
	v_cmp_nlt_f32_e32 vcc, s39, v38
	v_cmp_ngt_f32_e64 s[2:3], s6, v38
	s_or_b64 s[2:3], vcc, s[2:3]
	s_or_b64 s[4:5], s[2:3], s[4:5]
	v_cmp_nlt_f32_e32 vcc, s39, v39
	v_cmp_ngt_f32_e64 s[2:3], s6, v39
	s_or_b64 s[2:3], vcc, s[2:3]
	s_or_b64 s[4:5], s[2:3], s[4:5]
	v_cmp_nlt_f32_e32 vcc, s39, v40
	v_cmp_ngt_f32_e64 s[2:3], s6, v40
	s_or_b64 s[2:3], vcc, s[2:3]
	s_or_b64 s[4:5], s[2:3], s[4:5]
	v_cmp_nlt_f32_e32 vcc, s39, v41
	v_cmp_ngt_f32_e64 s[2:3], s6, v41
	s_or_b64 s[2:3], vcc, s[2:3]
	s_or_b64 s[4:5], s[2:3], s[4:5]
	v_cmp_nlt_f32_e32 vcc, s39, v42
	v_cmp_ngt_f32_e64 s[2:3], s6, v42
	s_or_b64 s[2:3], vcc, s[2:3]
	s_or_b64 s[4:5], s[2:3], s[4:5]
	v_cmp_nlt_f32_e32 vcc, s39, v43
	v_cmp_ngt_f32_e64 s[2:3], s6, v43
	s_or_b64 s[2:3], vcc, s[2:3]
	s_or_b64 s[4:5], s[2:3], s[4:5]
	v_cmp_nlt_f32_e32 vcc, s39, v44
	v_cmp_ngt_f32_e64 s[2:3], s6, v44
	s_or_b64 s[2:3], vcc, s[2:3]
	s_or_b64 s[4:5], s[2:3], s[4:5]
	v_cmp_nlt_f32_e32 vcc, s39, v45
	v_cmp_ngt_f32_e64 s[2:3], s6, v45
	s_or_b64 s[2:3], vcc, s[2:3]
	s_or_b64 s[4:5], s[2:3], s[4:5]
	v_cmp_nlt_f32_e32 vcc, s39, v46
	v_cmp_ngt_f32_e64 s[2:3], s6, v46
	s_or_b64 s[2:3], vcc, s[2:3]
	s_or_b64 s[4:5], s[2:3], s[4:5]
	v_cmp_nlt_f32_e32 vcc, s39, v47
	v_cmp_ngt_f32_e64 s[2:3], s6, v47
	s_or_b64 s[2:3], vcc, s[2:3]
	s_or_b64 s[4:5], s[2:3], s[4:5]
	v_cmp_nlt_f32_e32 vcc, s39, v48
	v_cmp_ngt_f32_e64 s[2:3], s6, v48
	s_or_b64 s[2:3], vcc, s[2:3]
	s_or_b64 s[4:5], s[2:3], s[4:5]
	v_cmp_nlt_f32_e32 vcc, s39, v49
	v_cmp_ngt_f32_e64 s[2:3], s6, v49
	s_or_b64 s[2:3], vcc, s[2:3]
	s_or_b64 s[2:3], s[2:3], s[4:5]
	v_cndmask_b32_e64 v0, 0, 1, s[2:3]
	v_cmp_ne_u32_e32 vcc, 0, v0
	s_cmp_lg_u64 vcc, 0
	s_cselect_b64 s[2:3], -1, 0
	v_cmp_eq_u32_e32 vcc, 0, v154
	s_and_b64 s[4:5], s[2:3], vcc
	s_and_saveexec_b64 s[2:3], s[4:5]
	v_mov_b32_e32 v0, s38
	ds_write_b32 v0, v252
	s_or_b64 exec, exec, s[2:3]
	s_and_b32 s2, s43, 0x3fffffc0
	s_lshl_b32 s2, s2, 2
	v_lshrrev_b32_e32 v51, 5, v154
	s_add_i32 s2, s2, 0
	v_cmp_eq_u32_e32 vcc, 0, v156
	v_lshl_add_u32 v50, v51, 4, s2
	s_and_saveexec_b64 s[2:3], vcc
	s_cbranch_execz .LBB0_669
	ds_write_b128 v50, v[34:37] offset:53376
	ds_write_b128 v50, v[38:41] offset:53408
	ds_write_b128 v50, v[42:45] offset:53440
	ds_write_b128 v50, v[46:49] offset:53472
